# v39 + mixer-internal grid barriers (FoX in->attn, NSA p0->p1->cmp tail->attn) replaced by hand-offs among the 32 workgroups of one batch element
# speedup vs baseline: 1.0039x; 1.0039x over previous
; __device__ __forceinline__ unsigned xb_ld(unsigned* p)              { return __hip_atomic_load(p, __ATOMIC_RELAXED, __HIP_MEMORY_SCOPE_AGENT); }
; __device__ __forceinline__ unsigned xb_add(unsigned* p, unsigned v) { return __hip_atomic_fetch_add(p, v, __ATOMIC_RELAXED, __HIP_MEMORY_SCOPE_AGENT); }
; #define XB_SPIN(cond, bar) do { unsigned _sp = 0; while (cond) { __builtin_amdgcn_s_sleep(1); \
;     if ((++_sp & 255u) == 0u) { if (xb_ld(&(bar)[XB_TMO])) break; if (_sp > XB_SPIN_CAP) { atomicAdd(&(bar)[XB_TMO], 1u); break; } } } } while (0)
; __device__ __forceinline__ void xcd_barrier(const XcdBarrier& b) {
;     asm volatile("s_waitcnt vmcnt(0)" ::: "memory");
;     __syncthreads();
;     if (threadIdx.x == 0) {
;         unsigned* bar = b.bar;
;         __builtin_amdgcn_s_waitcnt(0);
;         unsigned nloc = b.st[0], nx = b.st[1];
;         if (nloc == 0u) { xcd_barrier_complete(bar, b.x, nloc, nx); b.st[0] = nloc; b.st[1] = nx; }
;         const unsigned old = xb_add(&bar[XB_XSUB(b.x)], 1u);
;         const unsigned gen = old / nloc;
;         if (old + 1u == (gen + 1u) * nloc) {
;             __builtin_amdgcn_fence(__ATOMIC_RELEASE, "agent");
;             asm volatile("s_waitcnt vmcnt(0)" ::: "memory");
;             const unsigned og = xb_add(&bar[XB_TOP], 1u);
;             const unsigned tg = og / nx;
;             if (og + 1u == (tg + 1u) * nx) xb_add(&bar[XB_TOPGEN], 1u);
;             else XB_SPIN(xb_ld(&bar[XB_TOPGEN]) == tg, bar);
;             __builtin_amdgcn_fence(__ATOMIC_ACQUIRE, "agent");
;             xb_add(&bar[XB_XGEN(b.x)], 1u);
;             asm volatile("s_waitcnt vmcnt(0)" ::: "memory");
;         } else {
;             XB_SPIN(xb_ld(&bar[XB_XGEN(b.x)]) == gen, bar);
;             __builtin_amdgcn_fence(__ATOMIC_ACQUIRE, "agent");
;             asm volatile("s_waitcnt vmcnt(0)" ::: "memory");
;         }
;     }
;     __syncthreads();
; }
.LBB0_829:
	v_readlane_b32 s0, v253, 42
	v_readlane_b32 s4, v253, 32
	s_add_i32 s0, s0, 4
	v_readlane_b32 s7, v253, 35
	s_cmp_ge_i32 s0, s7
	v_readlane_b32 s5, v253, 33
	v_readlane_b32 s6, v253, 34
	s_cbranch_scc1 .LBB0_875
	v_readlane_b32 s40, v253, 36
	v_readlane_b32 s41, v253, 37
	s_mov_b32 s1, s76
	s_waitcnt vmcnt(0)
	s_waitcnt vmcnt(0) lgkmcnt(0)
	s_barrier
	s_mov_b64 s[42:43], exec
	v_readlane_b32 s4, v253, 53
	v_readlane_b32 s5, v253, 54
	s_and_b64 s[4:5], s[42:43], s[4:5]
	s_mov_b64 exec, s[4:5]
	s_cbranch_execz .LBB0_874
	v_readlane_b32 s10, v253, 36
	v_readlane_b32 s11, v253, 37
	v_readlane_b32 s14, v253, 55
	s_nop 3
	s_add_u32 s12, s10, 0x8000
	s_addc_u32 s13, s11, 0
	s_and_b32 s15, s88, 7
	s_lshl_b32 s15, s15, 8
	s_lshr_b32 s14, s14, 2
	s_add_i32 s14, s14, 1
	s_lshl_b32 s14, s14, 5
	v_mov_b32_e32 v2, s15
	v_mov_b32_e32 v5, 1
	global_atomic_add v2, v5, s[12:13]
	s_mov_b32 s18, 0
.Lgh_poll_LBB0_874:
	global_load_dword v6, v2, s[12:13] sc1
	s_waitcnt vmcnt(0)
	v_cmp_gt_u32_e32 vcc, s14, v6
	s_nop 3
	s_cmp_eq_u64 vcc, 0
	s_cbranch_scc1 .Lgh_done_LBB0_874
	s_add_i32 s18, s18, 1
	s_cmp_gt_u32 s18, 0x4000
	s_cbranch_scc1 .Lgh_done_LBB0_874
	s_sleep 1
	s_branch .Lgh_poll_LBB0_874
.Lgh_done_LBB0_874:
	buffer_inv sc1
	s_waitcnt vmcnt(0)
.LBB0_874:
	s_or_b64 exec, exec, s[42:43]
	s_waitcnt lgkmcnt(0)
	s_barrier

; __device__ __forceinline__ unsigned xb_ld(unsigned* p)              { return __hip_atomic_load(p, __ATOMIC_RELAXED, __HIP_MEMORY_SCOPE_AGENT); }
; __device__ __forceinline__ unsigned xb_add(unsigned* p, unsigned v) { return __hip_atomic_fetch_add(p, v, __ATOMIC_RELAXED, __HIP_MEMORY_SCOPE_AGENT); }
; #define XB_SPIN(cond, bar) do { unsigned _sp = 0; while (cond) { __builtin_amdgcn_s_sleep(1); \
;     if ((++_sp & 255u) == 0u) { if (xb_ld(&(bar)[XB_TMO])) break; if (_sp > XB_SPIN_CAP) { atomicAdd(&(bar)[XB_TMO], 1u); break; } } } } while (0)
; __device__ __forceinline__ void xcd_barrier(const XcdBarrier& b) {
;     asm volatile("s_waitcnt vmcnt(0)" ::: "memory");
;     __syncthreads();
;     if (threadIdx.x == 0) {
;         unsigned* bar = b.bar;
;         __builtin_amdgcn_s_waitcnt(0);
;         unsigned nloc = b.st[0], nx = b.st[1];
;         if (nloc == 0u) { xcd_barrier_complete(bar, b.x, nloc, nx); b.st[0] = nloc; b.st[1] = nx; }
;         const unsigned old = xb_add(&bar[XB_XSUB(b.x)], 1u);
;         const unsigned gen = old / nloc;
;         if (old + 1u == (gen + 1u) * nloc) {
;             __builtin_amdgcn_fence(__ATOMIC_RELEASE, "agent");
;             asm volatile("s_waitcnt vmcnt(0)" ::: "memory");
;             const unsigned og = xb_add(&bar[XB_TOP], 1u);
;             const unsigned tg = og / nx;
;             if (og + 1u == (tg + 1u) * nx) xb_add(&bar[XB_TOPGEN], 1u);
;             else XB_SPIN(xb_ld(&bar[XB_TOPGEN]) == tg, bar);
;             __builtin_amdgcn_fence(__ATOMIC_ACQUIRE, "agent");
;             xb_add(&bar[XB_XGEN(b.x)], 1u);
;             asm volatile("s_waitcnt vmcnt(0)" ::: "memory");
;         } else {
;             XB_SPIN(xb_ld(&bar[XB_XGEN(b.x)]) == gen, bar);
;             __builtin_amdgcn_fence(__ATOMIC_ACQUIRE, "agent");
;             asm volatile("s_waitcnt vmcnt(0)" ::: "memory");
;         }
;     }
;     __syncthreads();
; }
.LBB0_1177:
	s_waitcnt vmcnt(0)
	v_readlane_b32 s0, v253, 42
	v_readlane_b32 s4, v253, 32
	s_add_i32 s0, s0, 4
	v_readlane_b32 s7, v253, 35
	s_cmp_ge_i32 s0, s7
	v_readlane_b32 s5, v253, 33
	v_readlane_b32 s6, v253, 34
	s_barrier
	s_cbranch_scc1 .LBB0_1225
	v_readlane_b32 s34, v253, 36
	v_readlane_b32 s35, v253, 37
	s_mov_b32 s1, s76
	s_waitcnt vmcnt(0)
	s_waitcnt vmcnt(0) lgkmcnt(0)
	s_barrier
	s_mov_b64 s[38:39], exec
	v_readlane_b32 s2, v253, 53
	v_readlane_b32 s3, v253, 54
	s_and_b64 s[2:3], s[38:39], s[2:3]
	s_mov_b64 exec, s[2:3]
	s_cbranch_execz .LBB0_1224
	v_readlane_b32 s10, v253, 36
	v_readlane_b32 s11, v253, 37
	v_readlane_b32 s14, v253, 55
	s_nop 3
	s_add_u32 s12, s10, 0x8800
	s_addc_u32 s13, s11, 0
	s_and_b32 s15, s88, 7
	s_lshl_b32 s15, s15, 8
	s_lshr_b32 s14, s14, 2
	s_add_i32 s14, s14, 1
	s_lshl_b32 s14, s14, 5
	v_mov_b32_e32 v2, s15
	v_mov_b32_e32 v5, 1
	global_atomic_add v2, v5, s[12:13]
	s_mov_b32 s18, 0

; __device__ __forceinline__ unsigned xb_ld(unsigned* p)              { return __hip_atomic_load(p, __ATOMIC_RELAXED, __HIP_MEMORY_SCOPE_AGENT); }
; __device__ __forceinline__ unsigned xb_add(unsigned* p, unsigned v) { return __hip_atomic_fetch_add(p, v, __ATOMIC_RELAXED, __HIP_MEMORY_SCOPE_AGENT); }
; #define XB_SPIN(cond, bar) do { unsigned _sp = 0; while (cond) { __builtin_amdgcn_s_sleep(1); \
;     if ((++_sp & 255u) == 0u) { if (xb_ld(&(bar)[XB_TMO])) break; if (_sp > XB_SPIN_CAP) { atomicAdd(&(bar)[XB_TMO], 1u); break; } } } } while (0)
; __device__ __forceinline__ void xcd_barrier(const XcdBarrier& b) {
;     asm volatile("s_waitcnt vmcnt(0)" ::: "memory");
;     __syncthreads();
;     if (threadIdx.x == 0) {
;         unsigned* bar = b.bar;
;         __builtin_amdgcn_s_waitcnt(0);
;         unsigned nloc = b.st[0], nx = b.st[1];
;         if (nloc == 0u) { xcd_barrier_complete(bar, b.x, nloc, nx); b.st[0] = nloc; b.st[1] = nx; }
;         const unsigned old = xb_add(&bar[XB_XSUB(b.x)], 1u);
;         const unsigned gen = old / nloc;
;         if (old + 1u == (gen + 1u) * nloc) {
;             __builtin_amdgcn_fence(__ATOMIC_RELEASE, "agent");
;             asm volatile("s_waitcnt vmcnt(0)" ::: "memory");
;             const unsigned og = xb_add(&bar[XB_TOP], 1u);
;             const unsigned tg = og / nx;
;             if (og + 1u == (tg + 1u) * nx) xb_add(&bar[XB_TOPGEN], 1u);
;             else XB_SPIN(xb_ld(&bar[XB_TOPGEN]) == tg, bar);
;             __builtin_amdgcn_fence(__ATOMIC_ACQUIRE, "agent");
;             xb_add(&bar[XB_XGEN(b.x)], 1u);
;             asm volatile("s_waitcnt vmcnt(0)" ::: "memory");
;         } else {
;             XB_SPIN(xb_ld(&bar[XB_XGEN(b.x)]) == gen, bar);
;             __builtin_amdgcn_fence(__ATOMIC_ACQUIRE, "agent");
;             asm volatile("s_waitcnt vmcnt(0)" ::: "memory");
;         }
;     }
;     __syncthreads();
; }
.Lgh_done_LBB0_1224:
	buffer_inv sc1
	s_waitcnt vmcnt(0)
	s_branch .LBB0_1224
.LBB0_1190:
	s_lshl_b32 s0, s17, 3
	s_lshr_b32 s1, s22, 1
	s_or_b32 s20, s1, s0
	s_bfe_u32 s0, s16, 0x10003
	s_or_b32 s18, s0, 4
	s_cbranch_execnz .LBB0_1153
.LBB0_1191:
	s_add_i32 s0, s22, -16
	s_andn2_b64 vcc, exec, s[2:3]
	s_cbranch_vccz .LBB0_1154
	s_branch .LBB0_1155
.LBB0_1224:
	s_or_b64 exec, exec, s[38:39]
	s_waitcnt lgkmcnt(0)
	s_barrier

; __device__ __forceinline__ unsigned xb_ld(unsigned* p)              { return __hip_atomic_load(p, __ATOMIC_RELAXED, __HIP_MEMORY_SCOPE_AGENT); }
; __device__ __forceinline__ unsigned xb_add(unsigned* p, unsigned v) { return __hip_atomic_fetch_add(p, v, __ATOMIC_RELAXED, __HIP_MEMORY_SCOPE_AGENT); }
; #define XB_SPIN(cond, bar) do { unsigned _sp = 0; while (cond) { __builtin_amdgcn_s_sleep(1); \
;     if ((++_sp & 255u) == 0u) { if (xb_ld(&(bar)[XB_TMO])) break; if (_sp > XB_SPIN_CAP) { atomicAdd(&(bar)[XB_TMO], 1u); break; } } } } while (0)
; __device__ __forceinline__ void xcd_barrier(const XcdBarrier& b) {
;     asm volatile("s_waitcnt vmcnt(0)" ::: "memory");
;     __syncthreads();
;     if (threadIdx.x == 0) {
;         unsigned* bar = b.bar;
;         __builtin_amdgcn_s_waitcnt(0);
;         unsigned nloc = b.st[0], nx = b.st[1];
;         if (nloc == 0u) { xcd_barrier_complete(bar, b.x, nloc, nx); b.st[0] = nloc; b.st[1] = nx; }
;         const unsigned old = xb_add(&bar[XB_XSUB(b.x)], 1u);
;         const unsigned gen = old / nloc;
;         if (old + 1u == (gen + 1u) * nloc) {
;             __builtin_amdgcn_fence(__ATOMIC_RELEASE, "agent");
;             asm volatile("s_waitcnt vmcnt(0)" ::: "memory");
;             const unsigned og = xb_add(&bar[XB_TOP], 1u);
;             const unsigned tg = og / nx;
;             if (og + 1u == (tg + 1u) * nx) xb_add(&bar[XB_TOPGEN], 1u);
;             else XB_SPIN(xb_ld(&bar[XB_TOPGEN]) == tg, bar);
;             __builtin_amdgcn_fence(__ATOMIC_ACQUIRE, "agent");
;             xb_add(&bar[XB_XGEN(b.x)], 1u);
;             asm volatile("s_waitcnt vmcnt(0)" ::: "memory");
;         } else {
;             XB_SPIN(xb_ld(&bar[XB_XGEN(b.x)]) == gen, bar);
;             __builtin_amdgcn_fence(__ATOMIC_ACQUIRE, "agent");
;             asm volatile("s_waitcnt vmcnt(0)" ::: "memory");
;         }
;     }
;     __syncthreads();
; }
.LBB0_1257:
	v_readlane_b32 s0, v253, 42
	v_readlane_b32 s4, v253, 32
	s_add_i32 s0, s0, 5
	v_readlane_b32 s7, v253, 35
	s_cmp_ge_i32 s0, s7
	v_readlane_b32 s5, v253, 33
	v_readlane_b32 s6, v253, 34
	s_cbranch_scc1 .LBB0_1303
	v_readlane_b32 s34, v253, 36
	v_readlane_b32 s35, v253, 37
	s_mov_b32 s1, s76
	s_waitcnt vmcnt(0)
	s_waitcnt vmcnt(0) lgkmcnt(0)
	s_barrier
	s_mov_b64 s[38:39], exec
	v_readlane_b32 s2, v253, 53
	v_readlane_b32 s3, v253, 54
	s_and_b64 s[2:3], s[38:39], s[2:3]
	s_mov_b64 exec, s[2:3]
	s_cbranch_execz .LBB0_1302
	v_readlane_b32 s10, v253, 36
	v_readlane_b32 s11, v253, 37
	v_readlane_b32 s14, v253, 55
	s_nop 3
	s_add_u32 s12, s10, 0x9000
	s_addc_u32 s13, s11, 0
	s_and_b32 s15, s88, 7
	s_lshl_b32 s15, s15, 8
	s_lshr_b32 s14, s14, 2
	s_add_i32 s14, s14, 1
	s_lshl_b32 s14, s14, 5
	v_mov_b32_e32 v2, s15
	v_mov_b32_e32 v5, 1
	global_atomic_add v2, v5, s[12:13]
	s_mov_b32 s18, 0

; __device__ __forceinline__ unsigned xb_ld(unsigned* p)              { return __hip_atomic_load(p, __ATOMIC_RELAXED, __HIP_MEMORY_SCOPE_AGENT); }
; __device__ __forceinline__ unsigned xb_add(unsigned* p, unsigned v) { return __hip_atomic_fetch_add(p, v, __ATOMIC_RELAXED, __HIP_MEMORY_SCOPE_AGENT); }
; #define XB_SPIN(cond, bar) do { unsigned _sp = 0; while (cond) { __builtin_amdgcn_s_sleep(1); \
;     if ((++_sp & 255u) == 0u) { if (xb_ld(&(bar)[XB_TMO])) break; if (_sp > XB_SPIN_CAP) { atomicAdd(&(bar)[XB_TMO], 1u); break; } } } } while (0)
; __device__ __forceinline__ void xcd_barrier(const XcdBarrier& b) {
;     asm volatile("s_waitcnt vmcnt(0)" ::: "memory");
;     __syncthreads();
;     if (threadIdx.x == 0) {
;         unsigned* bar = b.bar;
;         __builtin_amdgcn_s_waitcnt(0);
;         unsigned nloc = b.st[0], nx = b.st[1];
;         if (nloc == 0u) { xcd_barrier_complete(bar, b.x, nloc, nx); b.st[0] = nloc; b.st[1] = nx; }
;         const unsigned old = xb_add(&bar[XB_XSUB(b.x)], 1u);
;         const unsigned gen = old / nloc;
;         if (old + 1u == (gen + 1u) * nloc) {
;             __builtin_amdgcn_fence(__ATOMIC_RELEASE, "agent");
;             asm volatile("s_waitcnt vmcnt(0)" ::: "memory");
;             const unsigned og = xb_add(&bar[XB_TOP], 1u);
;             const unsigned tg = og / nx;
;             if (og + 1u == (tg + 1u) * nx) xb_add(&bar[XB_TOPGEN], 1u);
;             else XB_SPIN(xb_ld(&bar[XB_TOPGEN]) == tg, bar);
;             __builtin_amdgcn_fence(__ATOMIC_ACQUIRE, "agent");
;             xb_add(&bar[XB_XGEN(b.x)], 1u);
;             asm volatile("s_waitcnt vmcnt(0)" ::: "memory");
;         } else {
;             XB_SPIN(xb_ld(&bar[XB_XGEN(b.x)]) == gen, bar);
;             __builtin_amdgcn_fence(__ATOMIC_ACQUIRE, "agent");
;             asm volatile("s_waitcnt vmcnt(0)" ::: "memory");
;         }
;     }
;     __syncthreads();
; }
.Lgh_done_LBB0_1302:
	buffer_inv sc1
	s_waitcnt vmcnt(0)
.LBB0_1302:
	s_or_b64 exec, exec, s[38:39]
	s_waitcnt lgkmcnt(0)
	s_barrier

; __device__ __forceinline__ unsigned xb_ld(unsigned* p)              { return __hip_atomic_load(p, __ATOMIC_RELAXED, __HIP_MEMORY_SCOPE_AGENT); }
; __device__ __forceinline__ unsigned xb_add(unsigned* p, unsigned v) { return __hip_atomic_fetch_add(p, v, __ATOMIC_RELAXED, __HIP_MEMORY_SCOPE_AGENT); }
; #define XB_SPIN(cond, bar) do { unsigned _sp = 0; while (cond) { __builtin_amdgcn_s_sleep(1); \
;     if ((++_sp & 255u) == 0u) { if (xb_ld(&(bar)[XB_TMO])) break; if (_sp > XB_SPIN_CAP) { atomicAdd(&(bar)[XB_TMO], 1u); break; } } } } while (0)
; __device__ __forceinline__ void xcd_barrier(const XcdBarrier& b) {
;     asm volatile("s_waitcnt vmcnt(0)" ::: "memory");
;     __syncthreads();
;     if (threadIdx.x == 0) {
;         unsigned* bar = b.bar;
;         __builtin_amdgcn_s_waitcnt(0);
;         unsigned nloc = b.st[0], nx = b.st[1];
;         if (nloc == 0u) { xcd_barrier_complete(bar, b.x, nloc, nx); b.st[0] = nloc; b.st[1] = nx; }
;         const unsigned old = xb_add(&bar[XB_XSUB(b.x)], 1u);
;         const unsigned gen = old / nloc;
;         if (old + 1u == (gen + 1u) * nloc) {
;             __builtin_amdgcn_fence(__ATOMIC_RELEASE, "agent");
;             asm volatile("s_waitcnt vmcnt(0)" ::: "memory");
;             const unsigned og = xb_add(&bar[XB_TOP], 1u);
;             const unsigned tg = og / nx;
;             if (og + 1u == (tg + 1u) * nx) xb_add(&bar[XB_TOPGEN], 1u);
;             else XB_SPIN(xb_ld(&bar[XB_TOPGEN]) == tg, bar);
;             __builtin_amdgcn_fence(__ATOMIC_ACQUIRE, "agent");
;             xb_add(&bar[XB_XGEN(b.x)], 1u);
;             asm volatile("s_waitcnt vmcnt(0)" ::: "memory");
;         } else {
;             XB_SPIN(xb_ld(&bar[XB_XGEN(b.x)]) == gen, bar);
;             __builtin_amdgcn_fence(__ATOMIC_ACQUIRE, "agent");
;             asm volatile("s_waitcnt vmcnt(0)" ::: "memory");
;         }
;     }
;     __syncthreads();
; }
.LBB0_1313:
	v_readlane_b32 s0, v253, 42
	v_readlane_b32 s4, v253, 32
	s_add_i32 s0, s0, 6
	v_readlane_b32 s7, v253, 35
	s_cmp_ge_i32 s0, s7
	v_readlane_b32 s5, v253, 33
	v_readlane_b32 s6, v253, 34
	s_cbranch_scc1 .LBB0_1359
	v_readlane_b32 s34, v253, 36
	v_readlane_b32 s35, v253, 37
	s_mov_b32 s1, s76
	s_waitcnt vmcnt(0)
	s_waitcnt vmcnt(0)
	s_barrier
	s_mov_b64 s[36:37], exec
	v_readlane_b32 s2, v253, 53
	v_readlane_b32 s3, v253, 54
	s_and_b64 s[2:3], s[36:37], s[2:3]
	s_mov_b64 exec, s[2:3]
	s_cbranch_execz .LBB0_1358
	v_readlane_b32 s10, v253, 36
	v_readlane_b32 s11, v253, 37
	v_readlane_b32 s14, v253, 55
	s_nop 3
	s_add_u32 s12, s10, 0x9800
	s_addc_u32 s13, s11, 0
	s_and_b32 s15, s88, 7
	s_lshl_b32 s15, s15, 8
	s_lshr_b32 s14, s14, 2
	s_add_i32 s14, s14, 1
	s_lshl_b32 s14, s14, 5
	v_mov_b32_e32 v2, s15
	v_mov_b32_e32 v5, 1
	global_atomic_add v2, v5, s[12:13]
	s_mov_b32 s18, 0
